# E10: E9 + first K-iteration of the P1/P5/G1/G2 K-loops peeled with srcC=0 (the 128 accumulator-zeroing v_mov per unit removed)
# speedup vs baseline: 1.0061x; 1.0061x over previous
.LBB0_161:
	s_cmp_eq_u32 s56, 0
	s_cselect_b32 s22, s55, s54
	s_cselect_b32 s25, s36, s38
	s_cselect_b32 s26, s33, s37
	s_cselect_b32 s24, s54, s55
	s_cselect_b32 s30, s38, s36
	s_cselect_b32 s31, s37, s33
	s_ashr_i32 s23, s22, 31
	s_lshl_b64 s[22:23], s[22:23], 19
	s_add_u32 s22, s26, s22
	s_addc_u32 s23, s25, s23
	s_and_b64 s[26:27], s[4:5], exec
	s_cselect_b32 s28, s23, s1
	s_cselect_b32 s29, s22, s0
	s_ashr_i32 s25, s24, 31
	s_lshl_b64 s[24:25], s[24:25], 19
	s_add_u32 s24, s31, s24
	s_addc_u32 s25, s30, s25
	s_and_b64 s[26:27], s[4:5], exec
	s_cselect_b32 s30, s25, s7
	s_cselect_b32 s31, s24, s6
	s_add_u32 s0, s0, 0x40080
	s_addc_u32 s1, s1, 0
	s_add_u32 s34, s6, 0x100
	s_addc_u32 s35, s7, 0
	s_mov_b32 s59, -2
	s_waitcnt vmcnt(0)
	ds_read_b128 v[130:133], v163
	ds_read_b128 v[134:137], v163 offset:1024
	ds_read_b128 v[138:141], v163 offset:2048
	ds_read_b128 v[142:145], v163 offset:3072
	ds_read_b128 v[184:187], v167
	ds_read_b128 v[188:191], v167 offset:1024
	ds_read_b128 v[192:195], v167 offset:2048
	ds_read_b128 v[196:199], v167 offset:3072
	s_add_u32 s6, s0, 0xfffc0080
	s_addc_u32 s7, s1, -1
	s_cmp_eq_u32 s59, 12
	s_cselect_b32 s27, s28, s7
	s_cselect_b32 s26, s29, s6
	s_cselect_b32 s7, s30, s35
	s_cselect_b32 s6, s31, s34
	v_lshl_add_u64 v[224:225], s[0:1], 0, v[176:177]
	s_add_i32 m0, s40, 0xc000
	ds_read_b128 v[200:203], v171
	ds_read_b128 v[204:207], v171 offset:1024
	ds_read_b128 v[208:211], v171 offset:2048
	ds_read_b128 v[212:215], v171 offset:3072
	ds_read_b128 v[216:219], v171 offset:4096
	ds_read_b128 v[220:223], v171 offset:5120
	ds_read_b128 v[228:231], v171 offset:6144
	ds_read_b128 v[232:235], v171 offset:7168
	global_load_lds_dwordx4 v[224:225], off
	v_lshl_add_u64 v[224:225], s[0:1], 0, v[178:179]
	s_add_i32 m0, s40, 0xe000
	s_nop 0
	global_load_lds_dwordx4 v[224:225], off
	s_waitcnt vmcnt(8)
	s_waitcnt lgkmcnt(0)
	s_barrier
	s_setprio 1
	s_waitcnt lgkmcnt(0)
	v_mfma_i32_16x16x64_i8 v[126:129], v[130:133], v[200:203], 0
	v_mfma_i32_16x16x64_i8 v[122:125], v[138:141], v[200:203], 0
	v_mfma_i32_16x16x64_i8 v[110:113], v[130:133], v[208:211], 0
	v_mfma_i32_16x16x64_i8 v[106:109], v[138:141], v[208:211], 0
	v_mfma_i32_16x16x64_i8 v[94:97], v[130:133], v[216:219], 0
	v_mfma_i32_16x16x64_i8 v[90:93], v[138:141], v[216:219], 0
	v_mfma_i32_16x16x64_i8 v[78:81], v[130:133], v[228:231], 0
	v_mfma_i32_16x16x64_i8 v[74:77], v[138:141], v[228:231], 0
	v_mfma_i32_16x16x64_i8 v[126:129], v[134:137], v[204:207], v[126:129]
	v_mfma_i32_16x16x64_i8 v[122:125], v[142:145], v[204:207], v[122:125]
	v_mfma_i32_16x16x64_i8 v[110:113], v[134:137], v[212:215], v[110:113]
	v_mfma_i32_16x16x64_i8 v[106:109], v[142:145], v[212:215], v[106:109]
	v_mfma_i32_16x16x64_i8 v[94:97], v[134:137], v[220:223], v[94:97]
	v_mfma_i32_16x16x64_i8 v[90:93], v[142:145], v[220:223], v[90:93]
	v_mfma_i32_16x16x64_i8 v[78:81], v[134:137], v[232:235], v[78:81]
	v_mfma_i32_16x16x64_i8 v[74:77], v[142:145], v[232:235], v[74:77]
	s_setprio 0
	s_setprio 1
	v_mfma_i32_16x16x64_i8 v[118:121], v[184:187], v[200:203], 0
	v_mfma_i32_16x16x64_i8 v[114:117], v[192:195], v[200:203], 0
	v_mfma_i32_16x16x64_i8 v[102:105], v[184:187], v[208:211], 0
	v_mfma_i32_16x16x64_i8 v[98:101], v[192:195], v[208:211], 0
	v_mfma_i32_16x16x64_i8 v[86:89], v[184:187], v[216:219], 0
	v_mfma_i32_16x16x64_i8 v[82:85], v[192:195], v[216:219], 0
	v_mfma_i32_16x16x64_i8 v[70:73], v[184:187], v[228:231], 0
	v_mfma_i32_16x16x64_i8 v[66:69], v[192:195], v[228:231], 0
	v_mfma_i32_16x16x64_i8 v[118:121], v[188:191], v[204:207], v[118:121]
	v_mfma_i32_16x16x64_i8 v[114:117], v[196:199], v[204:207], v[114:117]
	v_mfma_i32_16x16x64_i8 v[102:105], v[188:191], v[212:215], v[102:105]
	v_mfma_i32_16x16x64_i8 v[98:101], v[196:199], v[212:215], v[98:101]
	v_mfma_i32_16x16x64_i8 v[86:89], v[188:191], v[220:223], v[86:89]
	v_mfma_i32_16x16x64_i8 v[82:85], v[196:199], v[220:223], v[82:85]
	v_mfma_i32_16x16x64_i8 v[70:73], v[188:191], v[232:235], v[70:73]
	v_mfma_i32_16x16x64_i8 v[66:69], v[196:199], v[232:235], v[66:69]
	s_setprio 0
	s_barrier
	s_add_i32 s60, s51, s39
	v_lshl_add_u64 v[224:225], s[6:7], 0, v[148:149]
	s_mov_b32 m0, s60
	ds_read_b128 v[200:203], v171 offset:16384
	ds_read_b128 v[204:207], v171 offset:17408
	ds_read_b128 v[208:211], v171 offset:18432
	ds_read_b128 v[212:215], v171 offset:19456
	ds_read_b128 v[216:219], v171 offset:20480
	ds_read_b128 v[220:223], v171 offset:21504
	ds_read_b128 v[228:231], v171 offset:22528
	ds_read_b128 v[232:235], v171 offset:23552
	global_load_lds_dwordx4 v[224:225], off
	s_add_i32 m0, s60, 0x2000
	s_add_u32 s60, s6, 0x40000
	v_lshl_add_u64 v[236:237], s[6:7], 0, v[152:153]
	s_addc_u32 s61, s7, 0
	s_add_i32 s62, s52, s39
	global_load_lds_dwordx4 v[236:237], off
	v_lshl_add_u64 v[238:239], s[60:61], 0, v[148:149]
	s_mov_b32 m0, s62
	v_lshl_add_u64 v[240:241], s[26:27], 0, v[150:151]
	global_load_lds_dwordx4 v[238:239], off
	v_lshl_add_u64 v[238:239], s[60:61], 0, v[152:153]
	s_add_i32 m0, s62, 0x2000
	s_nop 0
	global_load_lds_dwordx4 v[238:239], off
	v_lshl_add_u64 v[238:239], s[26:27], 0, v[146:147]
	s_mov_b32 m0, s40
	s_nop 0
	global_load_lds_dwordx4 v[238:239], off
	s_mov_b32 m0, s41
	s_nop 0
	global_load_lds_dwordx4 v[240:241], off
	s_waitcnt vmcnt(8)
	s_waitcnt lgkmcnt(0)
	s_barrier
	s_setprio 1
	s_waitcnt lgkmcnt(0)
	v_mfma_i32_16x16x64_i8 v[62:65], v[130:133], v[200:203], 0
	v_mfma_i32_16x16x64_i8 v[58:61], v[138:141], v[200:203], 0
	v_mfma_i32_16x16x64_i8 v[46:49], v[130:133], v[208:211], 0
	v_mfma_i32_16x16x64_i8 v[42:45], v[138:141], v[208:211], 0
	v_mfma_i32_16x16x64_i8 v[30:33], v[130:133], v[216:219], 0
	v_mfma_i32_16x16x64_i8 v[26:29], v[138:141], v[216:219], 0
	v_mfma_i32_16x16x64_i8 v[14:17], v[130:133], v[228:231], 0
	v_mfma_i32_16x16x64_i8 v[10:13], v[138:141], v[228:231], 0
	v_mfma_i32_16x16x64_i8 v[62:65], v[134:137], v[204:207], v[62:65]
	v_mfma_i32_16x16x64_i8 v[58:61], v[142:145], v[204:207], v[58:61]
	v_mfma_i32_16x16x64_i8 v[46:49], v[134:137], v[212:215], v[46:49]
	v_mfma_i32_16x16x64_i8 v[42:45], v[142:145], v[212:215], v[42:45]
	v_mfma_i32_16x16x64_i8 v[30:33], v[134:137], v[220:223], v[30:33]
	v_mfma_i32_16x16x64_i8 v[26:29], v[142:145], v[220:223], v[26:29]
	v_mfma_i32_16x16x64_i8 v[14:17], v[134:137], v[232:235], v[14:17]
	v_mfma_i32_16x16x64_i8 v[10:13], v[142:145], v[232:235], v[10:13]
	s_setprio 0
	s_setprio 1
	v_mfma_i32_16x16x64_i8 v[54:57], v[184:187], v[200:203], 0
	v_mfma_i32_16x16x64_i8 v[50:53], v[192:195], v[200:203], 0
	v_mfma_i32_16x16x64_i8 v[38:41], v[184:187], v[208:211], 0
	v_mfma_i32_16x16x64_i8 v[34:37], v[192:195], v[208:211], 0
	v_mfma_i32_16x16x64_i8 v[22:25], v[184:187], v[216:219], 0
	v_mfma_i32_16x16x64_i8 v[18:21], v[192:195], v[216:219], 0
	v_mfma_i32_16x16x64_i8 v[6:9], v[184:187], v[228:231], 0
	v_mfma_i32_16x16x64_i8 v[2:5], v[192:195], v[228:231], 0
	v_mfma_i32_16x16x64_i8 v[54:57], v[188:191], v[204:207], v[54:57]
	v_mfma_i32_16x16x64_i8 v[50:53], v[196:199], v[204:207], v[50:53]
	v_mfma_i32_16x16x64_i8 v[38:41], v[188:191], v[212:215], v[38:41]
	v_mfma_i32_16x16x64_i8 v[34:37], v[196:199], v[212:215], v[34:37]
	v_mfma_i32_16x16x64_i8 v[22:25], v[188:191], v[220:223], v[22:25]
	v_mfma_i32_16x16x64_i8 v[18:21], v[196:199], v[220:223], v[18:21]
	v_mfma_i32_16x16x64_i8 v[6:9], v[188:191], v[232:235], v[6:9]
	v_mfma_i32_16x16x64_i8 v[2:5], v[196:199], v[232:235], v[2:5]
	s_setprio 0
	s_barrier
	s_add_i32 s60, 0, 0x18000
	v_add_u32_e32 v0, s60, v159
	s_add_i32 s61, 0, 0x1c000
	ds_read_b128 v[130:133], v0
	ds_read_b128 v[134:137], v0 offset:1024
	ds_read_b128 v[138:141], v0 offset:2048
	ds_read_b128 v[142:145], v0 offset:3072
	v_add_u32_e32 v0, s61, v159
	ds_read_b128 v[184:187], v0
	ds_read_b128 v[188:191], v0 offset:1024
	ds_read_b128 v[192:195], v0 offset:2048
	ds_read_b128 v[196:199], v0 offset:3072
	s_add_u32 s26, s26, 0x40000
	s_addc_u32 s27, s27, 0
	s_mov_b32 m0, s42
	v_lshl_add_u64 v[242:243], s[26:27], 0, v[146:147]
	ds_read_b128 v[200:203], v171 offset:32768
	ds_read_b128 v[204:207], v171 offset:33792
	ds_read_b128 v[208:211], v171 offset:34816
	ds_read_b128 v[212:215], v171 offset:35840
	ds_read_b128 v[216:219], v171 offset:36864
	ds_read_b128 v[220:223], v171 offset:37888
	ds_read_b128 v[228:231], v171 offset:38912
	ds_read_b128 v[232:235], v171 offset:39936
	global_load_lds_dwordx4 v[242:243], off
	v_lshl_add_u64 v[242:243], s[26:27], 0, v[150:151]
	s_mov_b32 m0, s43
	s_nop 0
	global_load_lds_dwordx4 v[242:243], off
	s_waitcnt vmcnt(8)
	s_waitcnt lgkmcnt(0)
	s_barrier
	s_setprio 1
	s_waitcnt lgkmcnt(0)
	v_mfma_i32_16x16x64_i8 v[126:129], v[130:133], v[200:203], v[126:129]
	v_mfma_i32_16x16x64_i8 v[122:125], v[138:141], v[200:203], v[122:125]
	v_mfma_i32_16x16x64_i8 v[110:113], v[130:133], v[208:211], v[110:113]
	v_mfma_i32_16x16x64_i8 v[106:109], v[138:141], v[208:211], v[106:109]
	v_mfma_i32_16x16x64_i8 v[94:97], v[130:133], v[216:219], v[94:97]
	v_mfma_i32_16x16x64_i8 v[90:93], v[138:141], v[216:219], v[90:93]
	v_mfma_i32_16x16x64_i8 v[78:81], v[130:133], v[228:231], v[78:81]
	v_mfma_i32_16x16x64_i8 v[74:77], v[138:141], v[228:231], v[74:77]
	v_mfma_i32_16x16x64_i8 v[126:129], v[134:137], v[204:207], v[126:129]
	v_mfma_i32_16x16x64_i8 v[122:125], v[142:145], v[204:207], v[122:125]
	v_mfma_i32_16x16x64_i8 v[110:113], v[134:137], v[212:215], v[110:113]
	v_mfma_i32_16x16x64_i8 v[106:109], v[142:145], v[212:215], v[106:109]
	v_mfma_i32_16x16x64_i8 v[94:97], v[134:137], v[220:223], v[94:97]
	v_mfma_i32_16x16x64_i8 v[90:93], v[142:145], v[220:223], v[90:93]
	v_mfma_i32_16x16x64_i8 v[78:81], v[134:137], v[232:235], v[78:81]
	v_mfma_i32_16x16x64_i8 v[74:77], v[142:145], v[232:235], v[74:77]
	s_setprio 0
	s_setprio 1
	v_mfma_i32_16x16x64_i8 v[118:121], v[184:187], v[200:203], v[118:121]
	v_mfma_i32_16x16x64_i8 v[114:117], v[192:195], v[200:203], v[114:117]
	v_mfma_i32_16x16x64_i8 v[102:105], v[184:187], v[208:211], v[102:105]
	v_mfma_i32_16x16x64_i8 v[98:101], v[192:195], v[208:211], v[98:101]
	v_mfma_i32_16x16x64_i8 v[86:89], v[184:187], v[216:219], v[86:89]
	v_mfma_i32_16x16x64_i8 v[82:85], v[192:195], v[216:219], v[82:85]
	v_mfma_i32_16x16x64_i8 v[70:73], v[184:187], v[228:231], v[70:73]
	v_mfma_i32_16x16x64_i8 v[66:69], v[192:195], v[228:231], v[66:69]
	v_mfma_i32_16x16x64_i8 v[118:121], v[188:191], v[204:207], v[118:121]
	v_mfma_i32_16x16x64_i8 v[114:117], v[196:199], v[204:207], v[114:117]
	v_mfma_i32_16x16x64_i8 v[102:105], v[188:191], v[212:215], v[102:105]
	v_mfma_i32_16x16x64_i8 v[98:101], v[196:199], v[212:215], v[98:101]
	v_mfma_i32_16x16x64_i8 v[86:89], v[188:191], v[220:223], v[86:89]
	v_mfma_i32_16x16x64_i8 v[82:85], v[196:199], v[220:223], v[82:85]
	v_mfma_i32_16x16x64_i8 v[70:73], v[188:191], v[232:235], v[70:73]
	v_mfma_i32_16x16x64_i8 v[66:69], v[196:199], v[232:235], v[66:69]
	s_setprio 0
	s_barrier
	s_add_i32 s26, s60, s39
	v_lshl_add_u64 v[224:225], v[224:225], 0, s[12:13]
	s_mov_b32 m0, s26
	ds_read_b128 v[200:203], v171 offset:49152
	ds_read_b128 v[204:207], v171 offset:50176
	ds_read_b128 v[208:211], v171 offset:51200
	ds_read_b128 v[212:215], v171 offset:52224
	ds_read_b128 v[216:219], v171 offset:53248
	ds_read_b128 v[220:223], v171 offset:54272
	ds_read_b128 v[228:231], v171 offset:55296
	ds_read_b128 v[232:235], v171 offset:56320
	global_load_lds_dwordx4 v[224:225], off
	s_add_i32 m0, s26, 0x2000
	s_add_u32 s6, s6, 0x40080
	v_lshl_add_u64 v[224:225], v[236:237], 0, s[12:13]
	s_addc_u32 s7, s7, 0
	s_add_i32 s26, s61, s39
	global_load_lds_dwordx4 v[224:225], off
	v_lshl_add_u64 v[224:225], s[6:7], 0, v[148:149]
	s_mov_b32 m0, s26
	s_nop 0
	global_load_lds_dwordx4 v[224:225], off
	v_lshl_add_u64 v[224:225], s[6:7], 0, v[152:153]
	s_add_i32 m0, s26, 0x2000
	s_nop 0
	global_load_lds_dwordx4 v[224:225], off
	v_lshl_add_u64 v[224:225], v[238:239], 0, s[12:13]
	s_mov_b32 m0, s45
	s_nop 0
	global_load_lds_dwordx4 v[224:225], off
	v_lshl_add_u64 v[224:225], v[240:241], 0, s[12:13]
	s_mov_b32 m0, s46
	s_nop 0
	global_load_lds_dwordx4 v[224:225], off
	s_waitcnt vmcnt(8)
	s_waitcnt lgkmcnt(0)
	s_barrier
	s_setprio 1
	s_waitcnt lgkmcnt(0)
	v_mfma_i32_16x16x64_i8 v[62:65], v[130:133], v[200:203], v[62:65]
	v_mfma_i32_16x16x64_i8 v[58:61], v[138:141], v[200:203], v[58:61]
	v_mfma_i32_16x16x64_i8 v[46:49], v[130:133], v[208:211], v[46:49]
	v_mfma_i32_16x16x64_i8 v[42:45], v[138:141], v[208:211], v[42:45]
	v_mfma_i32_16x16x64_i8 v[30:33], v[130:133], v[216:219], v[30:33]
	v_mfma_i32_16x16x64_i8 v[26:29], v[138:141], v[216:219], v[26:29]
	v_mfma_i32_16x16x64_i8 v[14:17], v[130:133], v[228:231], v[14:17]
	v_mfma_i32_16x16x64_i8 v[10:13], v[138:141], v[228:231], v[10:13]
	v_mfma_i32_16x16x64_i8 v[62:65], v[134:137], v[204:207], v[62:65]
	v_mfma_i32_16x16x64_i8 v[58:61], v[142:145], v[204:207], v[58:61]
	v_mfma_i32_16x16x64_i8 v[46:49], v[134:137], v[212:215], v[46:49]
	v_mfma_i32_16x16x64_i8 v[42:45], v[142:145], v[212:215], v[42:45]
	v_mfma_i32_16x16x64_i8 v[30:33], v[134:137], v[220:223], v[30:33]
	v_mfma_i32_16x16x64_i8 v[26:29], v[142:145], v[220:223], v[26:29]
	v_mfma_i32_16x16x64_i8 v[14:17], v[134:137], v[232:235], v[14:17]
	v_mfma_i32_16x16x64_i8 v[10:13], v[142:145], v[232:235], v[10:13]
	s_setprio 0
	s_setprio 1
	v_mfma_i32_16x16x64_i8 v[54:57], v[184:187], v[200:203], v[54:57]
	v_mfma_i32_16x16x64_i8 v[50:53], v[192:195], v[200:203], v[50:53]
	v_mfma_i32_16x16x64_i8 v[38:41], v[184:187], v[208:211], v[38:41]
	v_mfma_i32_16x16x64_i8 v[34:37], v[192:195], v[208:211], v[34:37]
	v_mfma_i32_16x16x64_i8 v[22:25], v[184:187], v[216:219], v[22:25]
	v_mfma_i32_16x16x64_i8 v[18:21], v[192:195], v[216:219], v[18:21]
	v_mfma_i32_16x16x64_i8 v[6:9], v[184:187], v[228:231], v[6:9]
	v_mfma_i32_16x16x64_i8 v[2:5], v[192:195], v[228:231], v[2:5]
	v_mfma_i32_16x16x64_i8 v[54:57], v[188:191], v[204:207], v[54:57]
	v_mfma_i32_16x16x64_i8 v[50:53], v[196:199], v[204:207], v[50:53]
	v_mfma_i32_16x16x64_i8 v[38:41], v[188:191], v[212:215], v[38:41]
	v_mfma_i32_16x16x64_i8 v[34:37], v[196:199], v[212:215], v[34:37]
	v_mfma_i32_16x16x64_i8 v[22:25], v[188:191], v[220:223], v[22:25]
	v_mfma_i32_16x16x64_i8 v[18:21], v[196:199], v[220:223], v[18:21]
	v_mfma_i32_16x16x64_i8 v[6:9], v[188:191], v[232:235], v[6:9]
	v_mfma_i32_16x16x64_i8 v[2:5], v[196:199], v[232:235], v[2:5]
	s_setprio 0
	s_barrier
	s_add_i32 s59, s59, 2
	s_add_u32 s0, s0, 0x100
	s_addc_u32 s1, s1, 0
	s_add_u32 s34, s34, 0x100
	s_addc_u32 s35, s35, 0
	s_cmp_gt_u32 s59, 13
	s_cbranch_scc0 .LBB0_162
	s_branch .Lkexit_162
	s_nop 0
	s_nop 0
	s_nop 0
	s_nop 0
	s_nop 0
	s_nop 0
	s_nop 0
	s_nop 0

.Lkexit_162:
	s_and_b64 vcc, exec, s[14:15]
	s_cbranch_vccz .LBB0_165
	s_barrier

.LBB0_981:
	s_ashr_i32 s11, s10, 31
	s_lshl_b64 s[12:13], s[10:11], 20
	s_add_u32 s12, s24, s12
	s_addc_u32 s13, s25, s13
	s_and_b64 s[14:15], s[4:5], exec
	s_cselect_b32 s11, s13, s19
	s_cselect_b32 s41, s12, s18
	s_ashr_i32 s9, s8, 31
	s_lshl_b64 s[14:15], s[8:9], 20
	s_add_u32 s14, s27, s14
	s_addc_u32 s15, s28, s15
	s_and_b64 s[22:23], s[4:5], exec
	s_cselect_b32 s9, s15, s21
	s_cselect_b32 s42, s14, s20
	s_add_u32 s18, s18, 0x80080
	s_addc_u32 s19, s19, 0
	s_add_u32 s43, s20, 0x100
	s_addc_u32 s44, s21, 0
	s_mov_b32 s45, -2
	ds_read_b128 v[146:149], v154
	ds_read_b128 v[158:161], v154 offset:1024
	ds_read_b128 v[162:165], v154 offset:2048
	ds_read_b128 v[166:169], v154 offset:3072
	ds_read_b128 v[170:173], v155
	ds_read_b128 v[174:177], v155 offset:1024
	ds_read_b128 v[178:181], v155 offset:2048
	ds_read_b128 v[182:185], v155 offset:3072
	s_add_u32 s20, s18, 0xfff80080
	s_addc_u32 s21, s19, -1
	s_cmp_eq_u32 s45, 28
	s_cselect_b32 s23, s11, s21
	s_cselect_b32 s22, s41, s20
	s_cselect_b32 s21, s9, s44
	s_cselect_b32 s20, s42, s43
	v_lshl_add_u64 v[150:151], s[18:19], 0, v[138:139]
	s_add_i32 m0, s17, 0xc000
	ds_read_b128 v[186:189], v156
	ds_read_b128 v[190:193], v156 offset:1024
	ds_read_b128 v[194:197], v156 offset:2048
	ds_read_b128 v[198:201], v156 offset:3072
	ds_read_b128 v[202:205], v156 offset:4096
	ds_read_b128 v[206:209], v156 offset:5120
	ds_read_b128 v[210:213], v156 offset:6144
	ds_read_b128 v[214:217], v156 offset:7168
	global_load_lds_dwordx4 v[150:151], off
	v_lshl_add_u64 v[150:151], s[18:19], 0, v[140:141]
	s_add_i32 m0, s17, 0xe000
	s_nop 0
	global_load_lds_dwordx4 v[150:151], off
	s_waitcnt vmcnt(8)
	s_waitcnt lgkmcnt(0)
	s_barrier
	s_setprio 1
	s_waitcnt lgkmcnt(0)
	v_mfma_f32_16x16x32_bf16 v[126:129], v[146:149], v[186:189], 0
	v_mfma_f32_16x16x32_bf16 v[122:125], v[162:165], v[186:189], 0
	v_mfma_f32_16x16x32_bf16 v[118:121], v[146:149], v[194:197], 0
	v_mfma_f32_16x16x32_bf16 v[114:117], v[162:165], v[194:197], 0
	v_mfma_f32_16x16x32_bf16 v[106:109], v[146:149], v[202:205], 0
	v_mfma_f32_16x16x32_bf16 v[98:101], v[162:165], v[202:205], 0
	v_mfma_f32_16x16x32_bf16 v[86:89], v[146:149], v[210:213], 0
	v_mfma_f32_16x16x32_bf16 v[78:81], v[162:165], v[210:213], 0
	v_mfma_f32_16x16x32_bf16 v[126:129], v[158:161], v[190:193], v[126:129]
	v_mfma_f32_16x16x32_bf16 v[122:125], v[166:169], v[190:193], v[122:125]
	v_mfma_f32_16x16x32_bf16 v[118:121], v[158:161], v[198:201], v[118:121]
	v_mfma_f32_16x16x32_bf16 v[114:117], v[166:169], v[198:201], v[114:117]
	v_mfma_f32_16x16x32_bf16 v[106:109], v[158:161], v[206:209], v[106:109]
	v_mfma_f32_16x16x32_bf16 v[98:101], v[166:169], v[206:209], v[98:101]
	v_mfma_f32_16x16x32_bf16 v[86:89], v[158:161], v[214:217], v[86:89]
	v_mfma_f32_16x16x32_bf16 v[78:81], v[166:169], v[214:217], v[78:81]
	s_setprio 0
	s_setprio 1
	v_mfma_f32_16x16x32_bf16 v[110:113], v[170:173], v[186:189], 0
	v_mfma_f32_16x16x32_bf16 v[102:105], v[178:181], v[186:189], 0
	v_mfma_f32_16x16x32_bf16 v[94:97], v[170:173], v[194:197], 0
	v_mfma_f32_16x16x32_bf16 v[90:93], v[178:181], v[194:197], 0
	v_mfma_f32_16x16x32_bf16 v[82:85], v[170:173], v[202:205], 0
	v_mfma_f32_16x16x32_bf16 v[74:77], v[178:181], v[202:205], 0
	v_mfma_f32_16x16x32_bf16 v[70:73], v[170:173], v[210:213], 0
	v_mfma_f32_16x16x32_bf16 v[66:69], v[178:181], v[210:213], 0
	v_mfma_f32_16x16x32_bf16 v[110:113], v[174:177], v[190:193], v[110:113]
	v_mfma_f32_16x16x32_bf16 v[102:105], v[182:185], v[190:193], v[102:105]
	v_mfma_f32_16x16x32_bf16 v[94:97], v[174:177], v[198:201], v[94:97]
	v_mfma_f32_16x16x32_bf16 v[90:93], v[182:185], v[198:201], v[90:93]
	v_mfma_f32_16x16x32_bf16 v[82:85], v[174:177], v[206:209], v[82:85]
	v_mfma_f32_16x16x32_bf16 v[74:77], v[182:185], v[206:209], v[74:77]
	v_mfma_f32_16x16x32_bf16 v[70:73], v[174:177], v[214:217], v[70:73]
	v_mfma_f32_16x16x32_bf16 v[66:69], v[182:185], v[214:217], v[66:69]
	s_setprio 0
	s_barrier
	s_add_i32 s46, s38, s29
	v_lshl_add_u64 v[150:151], s[20:21], 0, v[132:133]
	s_mov_b32 m0, s46
	ds_read_b128 v[186:189], v156 offset:16384
	ds_read_b128 v[190:193], v156 offset:17408
	ds_read_b128 v[194:197], v156 offset:18432
	ds_read_b128 v[198:201], v156 offset:19456
	ds_read_b128 v[202:205], v156 offset:20480
	ds_read_b128 v[206:209], v156 offset:21504
	ds_read_b128 v[210:213], v156 offset:22528
	ds_read_b128 v[214:217], v156 offset:23552
	global_load_lds_dwordx4 v[150:151], off
	s_add_i32 m0, s46, 0x2000
	s_add_u32 s46, s20, 0x80000
	v_lshl_add_u64 v[218:219], s[20:21], 0, v[136:137]
	s_addc_u32 s47, s21, 0
	s_add_i32 s48, s39, s29
	global_load_lds_dwordx4 v[218:219], off
	v_lshl_add_u64 v[220:221], s[46:47], 0, v[132:133]
	s_mov_b32 m0, s48
	v_lshl_add_u64 v[222:223], s[22:23], 0, v[134:135]
	global_load_lds_dwordx4 v[220:221], off
	v_lshl_add_u64 v[220:221], s[46:47], 0, v[136:137]
	s_add_i32 m0, s48, 0x2000
	s_nop 0
	global_load_lds_dwordx4 v[220:221], off
	v_lshl_add_u64 v[220:221], s[22:23], 0, v[130:131]
	s_mov_b32 m0, s17
	s_nop 0
	global_load_lds_dwordx4 v[220:221], off
	s_mov_b32 m0, s30
	s_nop 0
	global_load_lds_dwordx4 v[222:223], off
	s_waitcnt vmcnt(8)
	s_waitcnt lgkmcnt(0)
	s_barrier
	s_setprio 1
	s_waitcnt lgkmcnt(0)
	v_mfma_f32_16x16x32_bf16 v[62:65], v[146:149], v[186:189], 0
	v_mfma_f32_16x16x32_bf16 v[58:61], v[162:165], v[186:189], 0
	v_mfma_f32_16x16x32_bf16 v[50:53], v[146:149], v[194:197], 0
	v_mfma_f32_16x16x32_bf16 v[42:45], v[162:165], v[194:197], 0
	v_mfma_f32_16x16x32_bf16 v[38:41], v[146:149], v[202:205], 0
	v_mfma_f32_16x16x32_bf16 v[30:33], v[162:165], v[202:205], 0
	v_mfma_f32_16x16x32_bf16 v[22:25], v[146:149], v[210:213], 0
	v_mfma_f32_16x16x32_bf16 v[14:17], v[162:165], v[210:213], 0
	v_mfma_f32_16x16x32_bf16 v[62:65], v[158:161], v[190:193], v[62:65]
	v_mfma_f32_16x16x32_bf16 v[58:61], v[166:169], v[190:193], v[58:61]
	v_mfma_f32_16x16x32_bf16 v[50:53], v[158:161], v[198:201], v[50:53]
	v_mfma_f32_16x16x32_bf16 v[42:45], v[166:169], v[198:201], v[42:45]
	v_mfma_f32_16x16x32_bf16 v[38:41], v[158:161], v[206:209], v[38:41]
	v_mfma_f32_16x16x32_bf16 v[30:33], v[166:169], v[206:209], v[30:33]
	v_mfma_f32_16x16x32_bf16 v[22:25], v[158:161], v[214:217], v[22:25]
	v_mfma_f32_16x16x32_bf16 v[14:17], v[166:169], v[214:217], v[14:17]
	s_setprio 0
	s_setprio 1
	v_mfma_f32_16x16x32_bf16 v[54:57], v[170:173], v[186:189], 0
	v_mfma_f32_16x16x32_bf16 v[46:49], v[178:181], v[186:189], 0
	v_mfma_f32_16x16x32_bf16 v[34:37], v[170:173], v[194:197], 0
	v_mfma_f32_16x16x32_bf16 v[26:29], v[178:181], v[194:197], 0
	v_mfma_f32_16x16x32_bf16 v[18:21], v[170:173], v[202:205], 0
	v_mfma_f32_16x16x32_bf16 v[10:13], v[178:181], v[202:205], 0
	v_mfma_f32_16x16x32_bf16 v[6:9], v[170:173], v[210:213], 0
	v_mfma_f32_16x16x32_bf16 v[2:5], v[178:181], v[210:213], 0
	v_mfma_f32_16x16x32_bf16 v[54:57], v[174:177], v[190:193], v[54:57]
	v_mfma_f32_16x16x32_bf16 v[46:49], v[182:185], v[190:193], v[46:49]
	v_mfma_f32_16x16x32_bf16 v[34:37], v[174:177], v[198:201], v[34:37]
	v_mfma_f32_16x16x32_bf16 v[26:29], v[182:185], v[198:201], v[26:29]
	v_mfma_f32_16x16x32_bf16 v[18:21], v[174:177], v[206:209], v[18:21]
	v_mfma_f32_16x16x32_bf16 v[10:13], v[182:185], v[206:209], v[10:13]
	v_mfma_f32_16x16x32_bf16 v[6:9], v[174:177], v[214:217], v[6:9]
	v_mfma_f32_16x16x32_bf16 v[2:5], v[182:185], v[214:217], v[2:5]
	s_setprio 0
	s_barrier
	s_add_i32 s46, 0, 0x18000
	v_add_u32_e32 v0, s46, v152
	s_add_i32 s47, 0, 0x1c000
	ds_read_b128 v[146:149], v0
	ds_read_b128 v[158:161], v0 offset:1024
	ds_read_b128 v[162:165], v0 offset:2048
	ds_read_b128 v[166:169], v0 offset:3072
	v_add_u32_e32 v0, s47, v152
	ds_read_b128 v[170:173], v0
	ds_read_b128 v[174:177], v0 offset:1024
	ds_read_b128 v[178:181], v0 offset:2048
	ds_read_b128 v[182:185], v0 offset:3072
	s_add_u32 s22, s22, 0x80000
	s_addc_u32 s23, s23, 0
	s_mov_b32 m0, s31
	v_lshl_add_u64 v[224:225], s[22:23], 0, v[130:131]
	ds_read_b128 v[186:189], v156 offset:32768
	ds_read_b128 v[190:193], v156 offset:33792
	ds_read_b128 v[194:197], v156 offset:34816
	ds_read_b128 v[198:201], v156 offset:35840
	ds_read_b128 v[202:205], v156 offset:36864
	ds_read_b128 v[206:209], v156 offset:37888
	ds_read_b128 v[210:213], v156 offset:38912
	ds_read_b128 v[214:217], v156 offset:39936
	global_load_lds_dwordx4 v[224:225], off
	v_lshl_add_u64 v[224:225], s[22:23], 0, v[134:135]
	s_mov_b32 m0, s33
	s_nop 0
	global_load_lds_dwordx4 v[224:225], off
	s_waitcnt vmcnt(8)
	s_waitcnt lgkmcnt(0)
	s_barrier
	s_setprio 1
	s_waitcnt lgkmcnt(0)
	v_mfma_f32_16x16x32_bf16 v[126:129], v[146:149], v[186:189], v[126:129]
	v_mfma_f32_16x16x32_bf16 v[122:125], v[162:165], v[186:189], v[122:125]
	v_mfma_f32_16x16x32_bf16 v[118:121], v[146:149], v[194:197], v[118:121]
	v_mfma_f32_16x16x32_bf16 v[114:117], v[162:165], v[194:197], v[114:117]
	v_mfma_f32_16x16x32_bf16 v[106:109], v[146:149], v[202:205], v[106:109]
	v_mfma_f32_16x16x32_bf16 v[98:101], v[162:165], v[202:205], v[98:101]
	v_mfma_f32_16x16x32_bf16 v[86:89], v[146:149], v[210:213], v[86:89]
	v_mfma_f32_16x16x32_bf16 v[78:81], v[162:165], v[210:213], v[78:81]
	v_mfma_f32_16x16x32_bf16 v[126:129], v[158:161], v[190:193], v[126:129]
	v_mfma_f32_16x16x32_bf16 v[122:125], v[166:169], v[190:193], v[122:125]
	v_mfma_f32_16x16x32_bf16 v[118:121], v[158:161], v[198:201], v[118:121]
	v_mfma_f32_16x16x32_bf16 v[114:117], v[166:169], v[198:201], v[114:117]
	v_mfma_f32_16x16x32_bf16 v[106:109], v[158:161], v[206:209], v[106:109]
	v_mfma_f32_16x16x32_bf16 v[98:101], v[166:169], v[206:209], v[98:101]
	v_mfma_f32_16x16x32_bf16 v[86:89], v[158:161], v[214:217], v[86:89]
	v_mfma_f32_16x16x32_bf16 v[78:81], v[166:169], v[214:217], v[78:81]
	s_setprio 0
	s_setprio 1
	v_mfma_f32_16x16x32_bf16 v[110:113], v[170:173], v[186:189], v[110:113]
	v_mfma_f32_16x16x32_bf16 v[102:105], v[178:181], v[186:189], v[102:105]
	v_mfma_f32_16x16x32_bf16 v[94:97], v[170:173], v[194:197], v[94:97]
	v_mfma_f32_16x16x32_bf16 v[90:93], v[178:181], v[194:197], v[90:93]
	v_mfma_f32_16x16x32_bf16 v[82:85], v[170:173], v[202:205], v[82:85]
	v_mfma_f32_16x16x32_bf16 v[74:77], v[178:181], v[202:205], v[74:77]
	v_mfma_f32_16x16x32_bf16 v[70:73], v[170:173], v[210:213], v[70:73]
	v_mfma_f32_16x16x32_bf16 v[66:69], v[178:181], v[210:213], v[66:69]
	v_mfma_f32_16x16x32_bf16 v[110:113], v[174:177], v[190:193], v[110:113]
	v_mfma_f32_16x16x32_bf16 v[102:105], v[182:185], v[190:193], v[102:105]
	v_mfma_f32_16x16x32_bf16 v[94:97], v[174:177], v[198:201], v[94:97]
	v_mfma_f32_16x16x32_bf16 v[90:93], v[182:185], v[198:201], v[90:93]
	v_mfma_f32_16x16x32_bf16 v[82:85], v[174:177], v[206:209], v[82:85]
	v_mfma_f32_16x16x32_bf16 v[74:77], v[182:185], v[206:209], v[74:77]
	v_mfma_f32_16x16x32_bf16 v[70:73], v[174:177], v[214:217], v[70:73]
	v_mfma_f32_16x16x32_bf16 v[66:69], v[182:185], v[214:217], v[66:69]
	s_setprio 0
	s_barrier
	s_add_i32 s22, s46, s29
	v_lshl_add_u64 v[150:151], v[150:151], 0, s[2:3]
	s_mov_b32 m0, s22
	ds_read_b128 v[186:189], v156 offset:49152
	ds_read_b128 v[190:193], v156 offset:50176
	ds_read_b128 v[194:197], v156 offset:51200
	ds_read_b128 v[198:201], v156 offset:52224
	ds_read_b128 v[202:205], v156 offset:53248
	ds_read_b128 v[206:209], v156 offset:54272
	ds_read_b128 v[210:213], v156 offset:55296
	ds_read_b128 v[214:217], v156 offset:56320
	global_load_lds_dwordx4 v[150:151], off
	s_add_i32 m0, s22, 0x2000
	s_add_u32 s20, s20, 0x80080
	v_lshl_add_u64 v[150:151], v[218:219], 0, s[2:3]
	s_addc_u32 s21, s21, 0
	s_add_i32 s22, s47, s29
	global_load_lds_dwordx4 v[150:151], off
	v_lshl_add_u64 v[150:151], s[20:21], 0, v[132:133]
	s_mov_b32 m0, s22
	s_nop 0
	global_load_lds_dwordx4 v[150:151], off
	v_lshl_add_u64 v[150:151], s[20:21], 0, v[136:137]
	s_add_i32 m0, s22, 0x2000
	s_nop 0
	global_load_lds_dwordx4 v[150:151], off
	v_lshl_add_u64 v[150:151], v[220:221], 0, s[2:3]
	s_mov_b32 m0, s35
	s_nop 0
	global_load_lds_dwordx4 v[150:151], off
	v_lshl_add_u64 v[150:151], v[222:223], 0, s[2:3]
	s_mov_b32 m0, s36
	s_nop 0
	global_load_lds_dwordx4 v[150:151], off
	s_waitcnt vmcnt(8)
	s_waitcnt lgkmcnt(0)
	s_barrier
	s_setprio 1
	s_waitcnt lgkmcnt(0)
	v_mfma_f32_16x16x32_bf16 v[62:65], v[146:149], v[186:189], v[62:65]
	v_mfma_f32_16x16x32_bf16 v[58:61], v[162:165], v[186:189], v[58:61]
	v_mfma_f32_16x16x32_bf16 v[50:53], v[146:149], v[194:197], v[50:53]
	v_mfma_f32_16x16x32_bf16 v[42:45], v[162:165], v[194:197], v[42:45]
	v_mfma_f32_16x16x32_bf16 v[38:41], v[146:149], v[202:205], v[38:41]
	v_mfma_f32_16x16x32_bf16 v[30:33], v[162:165], v[202:205], v[30:33]
	v_mfma_f32_16x16x32_bf16 v[22:25], v[146:149], v[210:213], v[22:25]
	v_mfma_f32_16x16x32_bf16 v[14:17], v[162:165], v[210:213], v[14:17]
	v_mfma_f32_16x16x32_bf16 v[62:65], v[158:161], v[190:193], v[62:65]
	v_mfma_f32_16x16x32_bf16 v[58:61], v[166:169], v[190:193], v[58:61]
	v_mfma_f32_16x16x32_bf16 v[50:53], v[158:161], v[198:201], v[50:53]
	v_mfma_f32_16x16x32_bf16 v[42:45], v[166:169], v[198:201], v[42:45]
	v_mfma_f32_16x16x32_bf16 v[38:41], v[158:161], v[206:209], v[38:41]
	v_mfma_f32_16x16x32_bf16 v[30:33], v[166:169], v[206:209], v[30:33]
	v_mfma_f32_16x16x32_bf16 v[22:25], v[158:161], v[214:217], v[22:25]
	v_mfma_f32_16x16x32_bf16 v[14:17], v[166:169], v[214:217], v[14:17]
	s_setprio 0
	s_setprio 1
	v_mfma_f32_16x16x32_bf16 v[54:57], v[170:173], v[186:189], v[54:57]
	v_mfma_f32_16x16x32_bf16 v[46:49], v[178:181], v[186:189], v[46:49]
	v_mfma_f32_16x16x32_bf16 v[34:37], v[170:173], v[194:197], v[34:37]
	v_mfma_f32_16x16x32_bf16 v[26:29], v[178:181], v[194:197], v[26:29]
	v_mfma_f32_16x16x32_bf16 v[18:21], v[170:173], v[202:205], v[18:21]
	v_mfma_f32_16x16x32_bf16 v[10:13], v[178:181], v[202:205], v[10:13]
	v_mfma_f32_16x16x32_bf16 v[6:9], v[170:173], v[210:213], v[6:9]
	v_mfma_f32_16x16x32_bf16 v[2:5], v[178:181], v[210:213], v[2:5]
	v_mfma_f32_16x16x32_bf16 v[54:57], v[174:177], v[190:193], v[54:57]
	v_mfma_f32_16x16x32_bf16 v[46:49], v[182:185], v[190:193], v[46:49]
	v_mfma_f32_16x16x32_bf16 v[34:37], v[174:177], v[198:201], v[34:37]
	v_mfma_f32_16x16x32_bf16 v[26:29], v[182:185], v[198:201], v[26:29]
	v_mfma_f32_16x16x32_bf16 v[18:21], v[174:177], v[206:209], v[18:21]
	v_mfma_f32_16x16x32_bf16 v[10:13], v[182:185], v[206:209], v[10:13]
	v_mfma_f32_16x16x32_bf16 v[6:9], v[174:177], v[214:217], v[6:9]
	v_mfma_f32_16x16x32_bf16 v[2:5], v[182:185], v[214:217], v[2:5]
	s_setprio 0
	s_barrier
	s_add_i32 s45, s45, 2
	s_add_u32 s18, s18, 0x100
	s_addc_u32 s19, s19, 0
	s_add_u32 s43, s43, 0x100
	s_addc_u32 s44, s44, 0
	s_cmp_gt_u32 s45, 29
	s_cbranch_scc0 .LBB0_982
	s_branch .Lkexit_982
	s_nop 0
	s_nop 0
	s_nop 0
	s_nop 0
	s_nop 0
	s_nop 0
	s_nop 0
	s_nop 0

.Lkexit_982:
	s_and_b64 vcc, exec, s[6:7]
	s_cbranch_vccz .LBB0_985
	s_barrier

.LBB0_1213:
	s_add_u32 s35, s42, 0x100
	s_addc_u32 s37, s43, 0
	s_mov_b32 s39, -2
	s_mov_b64 s[42:43], 0
	ds_read_b128 v[70:73], v190
	ds_read_b128 v[74:77], v190 offset:1024
	ds_read_b128 v[78:81], v190 offset:2048
	ds_read_b128 v[82:85], v190 offset:3072
	ds_read_b128 v[94:97], v191
	ds_read_b128 v[98:101], v191 offset:1024
	ds_read_b128 v[102:105], v191 offset:2048
	ds_read_b128 v[106:109], v191 offset:3072
	s_add_u32 s44, s42, 0x100
	s_addc_u32 s45, s43, 0
	s_add_u32 s48, s35, s42
	s_addc_u32 s49, s37, s43
	s_cmp_eq_u32 s39, 12
	s_cselect_b64 vcc, -1, 0
	s_and_b64 s[46:47], vcc, exec
	s_cselect_b32 s73, 0, s44
	s_cselect_b32 s72, 0, s45
	s_cselect_b32 s46, s0, s48
	s_cselect_b32 s47, s1, s49
	s_add_u32 s48, s14, s73
	s_addc_u32 s49, s15, s72
	s_add_i32 m0, s11, 0xc000
	s_add_u32 s42, s24, s42
	s_addc_u32 s43, s25, s43
	ds_read_b128 v[176:179], v192
	ds_read_b128 v[180:183], v192 offset:1024
	ds_read_b128 v[194:197], v192 offset:2048
	ds_read_b128 v[198:201], v192 offset:3072
	ds_read_b128 v[202:205], v192 offset:4096
	ds_read_b128 v[206:209], v192 offset:5120
	ds_read_b128 v[210:213], v192 offset:6144
	ds_read_b128 v[214:217], v192 offset:7168
	global_load_lds_dwordx4 v187, s[42:43]
	s_add_i32 m0, s11, 0xe000
	v_mov_b32_e32 v0, v172
	global_load_lds_dwordx4 v186, s[42:43]
	v_mov_b32_e32 v169, v173
	v_lshlrev_b32_e32 v184, 11, v0
	v_lshlrev_b32_e32 v185, 11, v169
	v_bfe_u32 v0, v0, 16, 16
	v_bfe_u32 v169, v169, 16, 16
	v_and_b32_e32 v184, 0x7fff800, v184
	v_and_b32_e32 v185, 0x7fff800, v185
	v_lshl_add_u32 v0, v0, 11, v175
	v_lshl_add_u32 v169, v169, 11, v175
	v_add_u32_e32 v184, v184, v175
	v_add_u32_e32 v185, v185, v175
	v_cndmask_b32_e32 v168, v168, v0, vcc
	v_cndmask_b32_e32 v186, v186, v169, vcc
	v_cndmask_b32_e32 v170, v170, v184, vcc
	v_cndmask_b32_e32 v187, v187, v185, vcc
	s_waitcnt vmcnt(8)
	s_waitcnt lgkmcnt(0)
	s_barrier
	s_setprio 1
	s_waitcnt lgkmcnt(0)
	v_mfma_i32_16x16x64_i8 v[158:161], v[70:73], v[176:179], 0
	v_mfma_i32_16x16x64_i8 v[150:153], v[78:81], v[176:179], 0
	v_mfma_i32_16x16x64_i8 v[142:145], v[70:73], v[194:197], 0
	v_mfma_i32_16x16x64_i8 v[134:137], v[78:81], v[194:197], 0
	v_mfma_i32_16x16x64_i8 v[126:129], v[70:73], v[202:205], 0
	v_mfma_i32_16x16x64_i8 v[118:121], v[78:81], v[202:205], 0
	v_mfma_i32_16x16x64_i8 v[110:113], v[70:73], v[210:213], 0
	v_mfma_i32_16x16x64_i8 v[86:89], v[78:81], v[210:213], 0
	v_mfma_i32_16x16x64_i8 v[158:161], v[74:77], v[180:183], v[158:161]
	v_mfma_i32_16x16x64_i8 v[150:153], v[82:85], v[180:183], v[150:153]
	v_mfma_i32_16x16x64_i8 v[142:145], v[74:77], v[198:201], v[142:145]
	v_mfma_i32_16x16x64_i8 v[134:137], v[82:85], v[198:201], v[134:137]
	v_mfma_i32_16x16x64_i8 v[126:129], v[74:77], v[206:209], v[126:129]
	v_mfma_i32_16x16x64_i8 v[118:121], v[82:85], v[206:209], v[118:121]
	v_mfma_i32_16x16x64_i8 v[110:113], v[74:77], v[214:217], v[110:113]
	v_mfma_i32_16x16x64_i8 v[86:89], v[82:85], v[214:217], v[86:89]
	s_setprio 0
	s_setprio 1
	v_mfma_i32_16x16x64_i8 v[154:157], v[94:97], v[176:179], 0
	v_mfma_i32_16x16x64_i8 v[146:149], v[102:105], v[176:179], 0
	v_mfma_i32_16x16x64_i8 v[138:141], v[94:97], v[194:197], 0
	v_mfma_i32_16x16x64_i8 v[130:133], v[102:105], v[194:197], 0
	v_mfma_i32_16x16x64_i8 v[122:125], v[94:97], v[202:205], 0
	v_mfma_i32_16x16x64_i8 v[114:117], v[102:105], v[202:205], 0
	v_mfma_i32_16x16x64_i8 v[90:93], v[94:97], v[210:213], 0
	v_mfma_i32_16x16x64_i8 v[66:69], v[102:105], v[210:213], 0
	v_mfma_i32_16x16x64_i8 v[154:157], v[98:101], v[180:183], v[154:157]
	v_mfma_i32_16x16x64_i8 v[146:149], v[106:109], v[180:183], v[146:149]
	v_mfma_i32_16x16x64_i8 v[138:141], v[98:101], v[198:201], v[138:141]
	v_mfma_i32_16x16x64_i8 v[130:133], v[106:109], v[198:201], v[130:133]
	v_mfma_i32_16x16x64_i8 v[122:125], v[98:101], v[206:209], v[122:125]
	v_mfma_i32_16x16x64_i8 v[114:117], v[106:109], v[206:209], v[114:117]
	v_mfma_i32_16x16x64_i8 v[90:93], v[98:101], v[214:217], v[90:93]
	v_mfma_i32_16x16x64_i8 v[66:69], v[106:109], v[214:217], v[66:69]
	s_setprio 0
	s_barrier
	s_add_i32 s42, s67, s57
	v_lshl_add_u64 v[184:185], s[46:47], 0, v[164:165]
	s_mov_b32 m0, s42
	ds_read_b128 v[176:179], v192 offset:16384
	ds_read_b128 v[180:183], v192 offset:17408
	ds_read_b128 v[194:197], v192 offset:18432
	ds_read_b128 v[198:201], v192 offset:19456
	ds_read_b128 v[202:205], v192 offset:20480
	ds_read_b128 v[206:209], v192 offset:21504
	ds_read_b128 v[210:213], v192 offset:22528
	ds_read_b128 v[214:217], v192 offset:23552
	global_load_lds_dwordx4 v[184:185], off
	s_add_i32 m0, s42, 0x2000
	s_add_u32 s42, s46, 0x40000
	v_lshl_add_u64 v[218:219], s[46:47], 0, v[166:167]
	s_addc_u32 s43, s47, 0
	s_add_i32 s72, s68, s57
	global_load_lds_dwordx4 v[218:219], off
	v_lshl_add_u64 v[220:221], s[42:43], 0, v[164:165]
	s_mov_b32 m0, s72
	v_mov_b32_e32 v169, v171
	global_load_lds_dwordx4 v[220:221], off
	v_lshl_add_u64 v[220:221], s[42:43], 0, v[166:167]
	s_add_i32 m0, s72, 0x2000
	v_lshl_add_u64 v[222:223], s[48:49], 0, v[168:169]
	global_load_lds_dwordx4 v[220:221], off
	s_mov_b32 m0, s11
	v_lshl_add_u64 v[220:221], s[48:49], 0, v[170:171]
	global_load_lds_dwordx4 v170, s[48:49]
	s_mov_b32 m0, s58
	s_nop 0
	global_load_lds_dwordx4 v168, s[48:49]
	s_waitcnt vmcnt(8)
	s_waitcnt lgkmcnt(0)
	s_barrier
	s_setprio 1
	s_waitcnt lgkmcnt(0)
	v_mfma_i32_16x16x64_i8 v[62:65], v[70:73], v[176:179], 0
	v_mfma_i32_16x16x64_i8 v[54:57], v[78:81], v[176:179], 0
	v_mfma_i32_16x16x64_i8 v[46:49], v[70:73], v[194:197], 0
	v_mfma_i32_16x16x64_i8 v[38:41], v[78:81], v[194:197], 0
	v_mfma_i32_16x16x64_i8 v[30:33], v[70:73], v[202:205], 0
	v_mfma_i32_16x16x64_i8 v[22:25], v[78:81], v[202:205], 0
	v_mfma_i32_16x16x64_i8 v[14:17], v[70:73], v[210:213], 0
	v_mfma_i32_16x16x64_i8 v[6:9], v[78:81], v[210:213], 0
	v_mfma_i32_16x16x64_i8 v[62:65], v[74:77], v[180:183], v[62:65]
	v_mfma_i32_16x16x64_i8 v[54:57], v[82:85], v[180:183], v[54:57]
	v_mfma_i32_16x16x64_i8 v[46:49], v[74:77], v[198:201], v[46:49]
	v_mfma_i32_16x16x64_i8 v[38:41], v[82:85], v[198:201], v[38:41]
	v_mfma_i32_16x16x64_i8 v[30:33], v[74:77], v[206:209], v[30:33]
	v_mfma_i32_16x16x64_i8 v[22:25], v[82:85], v[206:209], v[22:25]
	v_mfma_i32_16x16x64_i8 v[14:17], v[74:77], v[214:217], v[14:17]
	v_mfma_i32_16x16x64_i8 v[6:9], v[82:85], v[214:217], v[6:9]
	s_setprio 0
	s_setprio 1
	v_mfma_i32_16x16x64_i8 v[58:61], v[94:97], v[176:179], 0
	v_mfma_i32_16x16x64_i8 v[50:53], v[102:105], v[176:179], 0
	v_mfma_i32_16x16x64_i8 v[42:45], v[94:97], v[194:197], 0
	v_mfma_i32_16x16x64_i8 v[34:37], v[102:105], v[194:197], 0
	v_mfma_i32_16x16x64_i8 v[26:29], v[94:97], v[202:205], 0
	v_mfma_i32_16x16x64_i8 v[18:21], v[102:105], v[202:205], 0
	v_mfma_i32_16x16x64_i8 v[10:13], v[94:97], v[210:213], 0
	v_mfma_i32_16x16x64_i8 v[2:5], v[102:105], v[210:213], 0
	v_mfma_i32_16x16x64_i8 v[58:61], v[98:101], v[180:183], v[58:61]
	v_mfma_i32_16x16x64_i8 v[50:53], v[106:109], v[180:183], v[50:53]
	v_mfma_i32_16x16x64_i8 v[42:45], v[98:101], v[198:201], v[42:45]
	v_mfma_i32_16x16x64_i8 v[34:37], v[106:109], v[198:201], v[34:37]
	v_mfma_i32_16x16x64_i8 v[26:29], v[98:101], v[206:209], v[26:29]
	v_mfma_i32_16x16x64_i8 v[18:21], v[106:109], v[206:209], v[18:21]
	v_mfma_i32_16x16x64_i8 v[10:13], v[98:101], v[214:217], v[10:13]
	v_mfma_i32_16x16x64_i8 v[2:5], v[106:109], v[214:217], v[2:5]
	s_setprio 0
	s_barrier
	s_add_i32 s42, 0, 0x18000
	v_add_u32_e32 v0, s42, v189
	s_add_i32 s72, 0, 0x1c000
	ds_read_b128 v[70:73], v0
	ds_read_b128 v[74:77], v0 offset:1024
	ds_read_b128 v[78:81], v0 offset:2048
	ds_read_b128 v[82:85], v0 offset:3072
	v_add_u32_e32 v0, s72, v189
	ds_read_b128 v[94:97], v0
	ds_read_b128 v[98:101], v0 offset:1024
	ds_read_b128 v[102:105], v0 offset:2048
	ds_read_b128 v[106:109], v0 offset:3072
	s_mov_b32 m0, s59
	ds_read_b128 v[176:179], v192 offset:32768
	ds_read_b128 v[180:183], v192 offset:33792
	ds_read_b128 v[194:197], v192 offset:34816
	ds_read_b128 v[198:201], v192 offset:35840
	ds_read_b128 v[202:205], v192 offset:36864
	ds_read_b128 v[206:209], v192 offset:37888
	ds_read_b128 v[210:213], v192 offset:38912
	ds_read_b128 v[214:217], v192 offset:39936
	global_load_lds_dwordx4 v187, s[48:49]
	s_mov_b32 m0, s60
	s_nop 0
	global_load_lds_dwordx4 v186, s[48:49]
	s_waitcnt vmcnt(8)
	s_waitcnt lgkmcnt(0)
	s_barrier
	s_setprio 1
	s_waitcnt lgkmcnt(0)
	v_mfma_i32_16x16x64_i8 v[158:161], v[70:73], v[176:179], v[158:161]
	v_mfma_i32_16x16x64_i8 v[150:153], v[78:81], v[176:179], v[150:153]
	v_mfma_i32_16x16x64_i8 v[142:145], v[70:73], v[194:197], v[142:145]
	v_mfma_i32_16x16x64_i8 v[134:137], v[78:81], v[194:197], v[134:137]
	v_mfma_i32_16x16x64_i8 v[126:129], v[70:73], v[202:205], v[126:129]
	v_mfma_i32_16x16x64_i8 v[118:121], v[78:81], v[202:205], v[118:121]
	v_mfma_i32_16x16x64_i8 v[110:113], v[70:73], v[210:213], v[110:113]
	v_mfma_i32_16x16x64_i8 v[86:89], v[78:81], v[210:213], v[86:89]
	v_mfma_i32_16x16x64_i8 v[158:161], v[74:77], v[180:183], v[158:161]
	v_mfma_i32_16x16x64_i8 v[150:153], v[82:85], v[180:183], v[150:153]
	v_mfma_i32_16x16x64_i8 v[142:145], v[74:77], v[198:201], v[142:145]
	v_mfma_i32_16x16x64_i8 v[134:137], v[82:85], v[198:201], v[134:137]
	v_mfma_i32_16x16x64_i8 v[126:129], v[74:77], v[206:209], v[126:129]
	v_mfma_i32_16x16x64_i8 v[118:121], v[82:85], v[206:209], v[118:121]
	v_mfma_i32_16x16x64_i8 v[110:113], v[74:77], v[214:217], v[110:113]
	v_mfma_i32_16x16x64_i8 v[86:89], v[82:85], v[214:217], v[86:89]
	s_setprio 0
	s_setprio 1
	v_mfma_i32_16x16x64_i8 v[154:157], v[94:97], v[176:179], v[154:157]
	v_mfma_i32_16x16x64_i8 v[146:149], v[102:105], v[176:179], v[146:149]
	v_mfma_i32_16x16x64_i8 v[138:141], v[94:97], v[194:197], v[138:141]
	v_mfma_i32_16x16x64_i8 v[130:133], v[102:105], v[194:197], v[130:133]
	v_mfma_i32_16x16x64_i8 v[122:125], v[94:97], v[202:205], v[122:125]
	v_mfma_i32_16x16x64_i8 v[114:117], v[102:105], v[202:205], v[114:117]
	v_mfma_i32_16x16x64_i8 v[90:93], v[94:97], v[210:213], v[90:93]
	v_mfma_i32_16x16x64_i8 v[66:69], v[102:105], v[210:213], v[66:69]
	v_mfma_i32_16x16x64_i8 v[154:157], v[98:101], v[180:183], v[154:157]
	v_mfma_i32_16x16x64_i8 v[146:149], v[106:109], v[180:183], v[146:149]
	v_mfma_i32_16x16x64_i8 v[138:141], v[98:101], v[198:201], v[138:141]
	v_mfma_i32_16x16x64_i8 v[130:133], v[106:109], v[198:201], v[130:133]
	v_mfma_i32_16x16x64_i8 v[122:125], v[98:101], v[206:209], v[122:125]
	v_mfma_i32_16x16x64_i8 v[114:117], v[106:109], v[206:209], v[114:117]
	v_mfma_i32_16x16x64_i8 v[90:93], v[98:101], v[214:217], v[90:93]
	v_mfma_i32_16x16x64_i8 v[66:69], v[106:109], v[214:217], v[66:69]
	s_setprio 0
	s_barrier
	s_add_i32 s42, s42, s57
	v_lshl_add_u64 v[184:185], v[184:185], 0, s[22:23]
	s_mov_b32 m0, s42
	ds_read_b128 v[176:179], v192 offset:49152
	ds_read_b128 v[180:183], v192 offset:50176
	ds_read_b128 v[194:197], v192 offset:51200
	ds_read_b128 v[198:201], v192 offset:52224
	ds_read_b128 v[202:205], v192 offset:53248
	ds_read_b128 v[206:209], v192 offset:54272
	ds_read_b128 v[210:213], v192 offset:55296
	ds_read_b128 v[214:217], v192 offset:56320
	global_load_lds_dwordx4 v[184:185], off
	s_add_i32 m0, s42, 0x2000
	s_add_u32 s42, s46, 0x40080
	v_lshl_add_u64 v[184:185], v[218:219], 0, s[22:23]
	s_addc_u32 s43, s47, 0
	s_add_i32 s46, s72, s57
	global_load_lds_dwordx4 v[184:185], off
	v_lshl_add_u64 v[184:185], s[42:43], 0, v[164:165]
	s_mov_b32 m0, s46
	s_nop 0
	global_load_lds_dwordx4 v[184:185], off
	v_lshl_add_u64 v[184:185], s[42:43], 0, v[166:167]
	s_add_i32 m0, s46, 0x2000
	s_nop 0
	global_load_lds_dwordx4 v[184:185], off
	v_lshl_add_u64 v[184:185], v[220:221], 0, s[22:23]
	s_mov_b32 m0, s63
	s_nop 0
	global_load_lds_dwordx4 v[184:185], off
	v_lshl_add_u64 v[184:185], v[222:223], 0, s[22:23]
	s_mov_b32 m0, s64
	s_nop 0
	global_load_lds_dwordx4 v[184:185], off
	s_waitcnt vmcnt(8)
	s_waitcnt lgkmcnt(0)
	s_barrier
	s_setprio 1
	s_waitcnt lgkmcnt(0)
	v_mfma_i32_16x16x64_i8 v[62:65], v[70:73], v[176:179], v[62:65]
	v_mfma_i32_16x16x64_i8 v[54:57], v[78:81], v[176:179], v[54:57]
	v_mfma_i32_16x16x64_i8 v[46:49], v[70:73], v[194:197], v[46:49]
	v_mfma_i32_16x16x64_i8 v[38:41], v[78:81], v[194:197], v[38:41]
	v_mfma_i32_16x16x64_i8 v[30:33], v[70:73], v[202:205], v[30:33]
	v_mfma_i32_16x16x64_i8 v[22:25], v[78:81], v[202:205], v[22:25]
	v_mfma_i32_16x16x64_i8 v[14:17], v[70:73], v[210:213], v[14:17]
	v_mfma_i32_16x16x64_i8 v[6:9], v[78:81], v[210:213], v[6:9]
	v_mfma_i32_16x16x64_i8 v[62:65], v[74:77], v[180:183], v[62:65]
	v_mfma_i32_16x16x64_i8 v[54:57], v[82:85], v[180:183], v[54:57]
	v_mfma_i32_16x16x64_i8 v[46:49], v[74:77], v[198:201], v[46:49]
	v_mfma_i32_16x16x64_i8 v[38:41], v[82:85], v[198:201], v[38:41]
	v_mfma_i32_16x16x64_i8 v[30:33], v[74:77], v[206:209], v[30:33]
	v_mfma_i32_16x16x64_i8 v[22:25], v[82:85], v[206:209], v[22:25]
	v_mfma_i32_16x16x64_i8 v[14:17], v[74:77], v[214:217], v[14:17]
	v_mfma_i32_16x16x64_i8 v[6:9], v[82:85], v[214:217], v[6:9]
	s_setprio 0
	s_setprio 1
	v_mfma_i32_16x16x64_i8 v[58:61], v[94:97], v[176:179], v[58:61]
	v_mfma_i32_16x16x64_i8 v[50:53], v[102:105], v[176:179], v[50:53]
	v_mfma_i32_16x16x64_i8 v[42:45], v[94:97], v[194:197], v[42:45]
	v_mfma_i32_16x16x64_i8 v[34:37], v[102:105], v[194:197], v[34:37]
	v_mfma_i32_16x16x64_i8 v[26:29], v[94:97], v[202:205], v[26:29]
	v_mfma_i32_16x16x64_i8 v[18:21], v[102:105], v[202:205], v[18:21]
	v_mfma_i32_16x16x64_i8 v[10:13], v[94:97], v[210:213], v[10:13]
	v_mfma_i32_16x16x64_i8 v[2:5], v[102:105], v[210:213], v[2:5]
	v_mfma_i32_16x16x64_i8 v[58:61], v[98:101], v[180:183], v[58:61]
	v_mfma_i32_16x16x64_i8 v[50:53], v[106:109], v[180:183], v[50:53]
	v_mfma_i32_16x16x64_i8 v[42:45], v[98:101], v[198:201], v[42:45]
	v_mfma_i32_16x16x64_i8 v[34:37], v[106:109], v[198:201], v[34:37]
	v_mfma_i32_16x16x64_i8 v[26:29], v[98:101], v[206:209], v[26:29]
	v_mfma_i32_16x16x64_i8 v[18:21], v[106:109], v[206:209], v[18:21]
	v_mfma_i32_16x16x64_i8 v[10:13], v[98:101], v[214:217], v[10:13]
	v_mfma_i32_16x16x64_i8 v[2:5], v[106:109], v[214:217], v[2:5]
	s_setprio 0
	s_barrier
	s_add_i32 s39, s39, 2
	s_cmp_gt_u32 s39, 13
	s_mov_b64 s[42:43], s[44:45]
	s_cbranch_scc0 .LBB0_1214
	s_branch .Lkexit_1214
	s_nop 0
	s_nop 0
	s_nop 0
	s_nop 0
	s_nop 0
	s_nop 0
	s_nop 0
	s_nop 0
	s_nop 0
	s_nop 0
	s_nop 0
	s_nop 0

.Lkexit_1214:
	s_and_b64 vcc, exec, s[26:27]
	s_cbranch_vccz .LBB0_1217
	s_barrier

.LBB0_1366:
	s_lshl_b64 s[36:37], s[28:29], 19
	s_add_u32 s36, s2, s36
	s_addc_u32 s37, s3, s37
	s_and_b64 s[0:1], exec, s[0:1]
	s_cselect_b32 s27, s37, s43
	s_cselect_b32 s29, s36, s42
	s_add_u32 s0, s42, 0x40080
	s_addc_u32 s1, s43, 0
	s_add_u32 s31, s40, 0x100
	s_addc_u32 s39, s41, 0
	s_mov_b32 s61, -2
	ds_read_b128 v[66:69], v229
	ds_read_b128 v[70:73], v229 offset:1024
	ds_read_b128 v[82:85], v229 offset:2048
	ds_read_b128 v[86:89], v229 offset:3072
	ds_read_b128 v[90:93], v230
	ds_read_b128 v[94:97], v230 offset:1024
	ds_read_b128 v[98:101], v230 offset:2048
	ds_read_b128 v[102:105], v230 offset:3072
	s_add_u32 s40, s0, 0xfffc0080
	s_addc_u32 s41, s1, -1
	s_cmp_eq_u32 s61, 12
	s_cselect_b32 s43, s27, s41
	s_cselect_b32 s42, s29, s40
	s_cselect_b32 s41, s35, s39
	s_cselect_b32 s40, s34, s31
	v_lshl_add_u64 v[208:209], s[0:1], 0, v[170:171]
	s_add_i32 m0, s15, 0xc000
	ds_read_b128 v[176:179], v231
	ds_read_b128 v[180:183], v231 offset:1024
	ds_read_b128 v[184:187], v231 offset:2048
	ds_read_b128 v[188:191], v231 offset:3072
	ds_read_b128 v[192:195], v231 offset:4096
	ds_read_b128 v[196:199], v231 offset:5120
	ds_read_b128 v[200:203], v231 offset:6144
	ds_read_b128 v[204:207], v231 offset:7168
	global_load_lds_dwordx4 v[208:209], off
	v_lshl_add_u64 v[208:209], s[0:1], 0, v[172:173]
	s_add_i32 m0, s15, 0xe000
	s_nop 0
	global_load_lds_dwordx4 v[208:209], off
	s_waitcnt vmcnt(8)
	s_waitcnt lgkmcnt(0)
	s_barrier
	s_setprio 1
	s_waitcnt lgkmcnt(0)
	v_mfma_i32_16x16x64_i8 v[158:161], v[66:69], v[176:179], 0
	v_mfma_i32_16x16x64_i8 v[154:157], v[82:85], v[176:179], 0
	v_mfma_i32_16x16x64_i8 v[142:145], v[66:69], v[184:187], 0
	v_mfma_i32_16x16x64_i8 v[138:141], v[82:85], v[184:187], 0
	v_mfma_i32_16x16x64_i8 v[126:129], v[66:69], v[192:195], 0
	v_mfma_i32_16x16x64_i8 v[122:125], v[82:85], v[192:195], 0
	v_mfma_i32_16x16x64_i8 v[110:113], v[66:69], v[200:203], 0
	v_mfma_i32_16x16x64_i8 v[106:109], v[82:85], v[200:203], 0
	v_mfma_i32_16x16x64_i8 v[158:161], v[70:73], v[180:183], v[158:161]
	v_mfma_i32_16x16x64_i8 v[154:157], v[86:89], v[180:183], v[154:157]
	v_mfma_i32_16x16x64_i8 v[142:145], v[70:73], v[188:191], v[142:145]
	v_mfma_i32_16x16x64_i8 v[138:141], v[86:89], v[188:191], v[138:141]
	v_mfma_i32_16x16x64_i8 v[126:129], v[70:73], v[196:199], v[126:129]
	v_mfma_i32_16x16x64_i8 v[122:125], v[86:89], v[196:199], v[122:125]
	v_mfma_i32_16x16x64_i8 v[110:113], v[70:73], v[204:207], v[110:113]
	v_mfma_i32_16x16x64_i8 v[106:109], v[86:89], v[204:207], v[106:109]
	s_setprio 0
	s_setprio 1
	v_mfma_i32_16x16x64_i8 v[150:153], v[90:93], v[176:179], 0
	v_mfma_i32_16x16x64_i8 v[146:149], v[98:101], v[176:179], 0
	v_mfma_i32_16x16x64_i8 v[134:137], v[90:93], v[184:187], 0
	v_mfma_i32_16x16x64_i8 v[130:133], v[98:101], v[184:187], 0
	v_mfma_i32_16x16x64_i8 v[118:121], v[90:93], v[192:195], 0
	v_mfma_i32_16x16x64_i8 v[114:117], v[98:101], v[192:195], 0
	v_mfma_i32_16x16x64_i8 v[78:81], v[90:93], v[200:203], 0
	v_mfma_i32_16x16x64_i8 v[74:77], v[98:101], v[200:203], 0
	v_mfma_i32_16x16x64_i8 v[150:153], v[94:97], v[180:183], v[150:153]
	v_mfma_i32_16x16x64_i8 v[146:149], v[102:105], v[180:183], v[146:149]
	v_mfma_i32_16x16x64_i8 v[134:137], v[94:97], v[188:191], v[134:137]
	v_mfma_i32_16x16x64_i8 v[130:133], v[102:105], v[188:191], v[130:133]
	v_mfma_i32_16x16x64_i8 v[118:121], v[94:97], v[196:199], v[118:121]
	v_mfma_i32_16x16x64_i8 v[114:117], v[102:105], v[196:199], v[114:117]
	v_mfma_i32_16x16x64_i8 v[78:81], v[94:97], v[204:207], v[78:81]
	v_mfma_i32_16x16x64_i8 v[74:77], v[102:105], v[204:207], v[74:77]
	s_setprio 0
	s_barrier
	s_add_i32 s62, s57, s47
	v_lshl_add_u64 v[208:209], s[40:41], 0, v[164:165]
	s_mov_b32 m0, s62
	ds_read_b128 v[176:179], v231 offset:16384
	ds_read_b128 v[180:183], v231 offset:17408
	ds_read_b128 v[184:187], v231 offset:18432
	ds_read_b128 v[188:191], v231 offset:19456
	ds_read_b128 v[192:195], v231 offset:20480
	ds_read_b128 v[196:199], v231 offset:21504
	ds_read_b128 v[200:203], v231 offset:22528
	ds_read_b128 v[204:207], v231 offset:23552
	global_load_lds_dwordx4 v[208:209], off
	s_add_i32 m0, s62, 0x2000
	s_add_u32 s62, s40, 0x40000
	v_lshl_add_u64 v[210:211], s[40:41], 0, v[168:169]
	s_addc_u32 s63, s41, 0
	s_add_i32 s64, s58, s47
	global_load_lds_dwordx4 v[210:211], off
	v_lshl_add_u64 v[212:213], s[62:63], 0, v[164:165]
	s_mov_b32 m0, s64
	v_lshl_add_u64 v[214:215], s[42:43], 0, v[166:167]
	global_load_lds_dwordx4 v[212:213], off
	v_lshl_add_u64 v[212:213], s[62:63], 0, v[168:169]
	s_add_i32 m0, s64, 0x2000
	s_nop 0
	global_load_lds_dwordx4 v[212:213], off
	v_lshl_add_u64 v[212:213], s[42:43], 0, v[162:163]
	s_mov_b32 m0, s15
	s_nop 0
	global_load_lds_dwordx4 v[212:213], off
	s_mov_b32 m0, s48
	s_nop 0
	global_load_lds_dwordx4 v[214:215], off
	s_waitcnt vmcnt(8)
	s_waitcnt lgkmcnt(0)
	s_barrier
	s_setprio 1
	s_waitcnt lgkmcnt(0)
	v_mfma_i32_16x16x64_i8 v[62:65], v[66:69], v[176:179], 0
	v_mfma_i32_16x16x64_i8 v[58:61], v[82:85], v[176:179], 0
	v_mfma_i32_16x16x64_i8 v[46:49], v[66:69], v[184:187], 0
	v_mfma_i32_16x16x64_i8 v[42:45], v[82:85], v[184:187], 0
	v_mfma_i32_16x16x64_i8 v[30:33], v[66:69], v[192:195], 0
	v_mfma_i32_16x16x64_i8 v[26:29], v[82:85], v[192:195], 0
	v_mfma_i32_16x16x64_i8 v[14:17], v[66:69], v[200:203], 0
	v_mfma_i32_16x16x64_i8 v[10:13], v[82:85], v[200:203], 0
	v_mfma_i32_16x16x64_i8 v[62:65], v[70:73], v[180:183], v[62:65]
	v_mfma_i32_16x16x64_i8 v[58:61], v[86:89], v[180:183], v[58:61]
	v_mfma_i32_16x16x64_i8 v[46:49], v[70:73], v[188:191], v[46:49]
	v_mfma_i32_16x16x64_i8 v[42:45], v[86:89], v[188:191], v[42:45]
	v_mfma_i32_16x16x64_i8 v[30:33], v[70:73], v[196:199], v[30:33]
	v_mfma_i32_16x16x64_i8 v[26:29], v[86:89], v[196:199], v[26:29]
	v_mfma_i32_16x16x64_i8 v[14:17], v[70:73], v[204:207], v[14:17]
	v_mfma_i32_16x16x64_i8 v[10:13], v[86:89], v[204:207], v[10:13]
	s_setprio 0
	s_setprio 1
	v_mfma_i32_16x16x64_i8 v[54:57], v[90:93], v[176:179], 0
	v_mfma_i32_16x16x64_i8 v[50:53], v[98:101], v[176:179], 0
	v_mfma_i32_16x16x64_i8 v[38:41], v[90:93], v[184:187], 0
	v_mfma_i32_16x16x64_i8 v[34:37], v[98:101], v[184:187], 0
	v_mfma_i32_16x16x64_i8 v[22:25], v[90:93], v[192:195], 0
	v_mfma_i32_16x16x64_i8 v[18:21], v[98:101], v[192:195], 0
	v_mfma_i32_16x16x64_i8 v[6:9], v[90:93], v[200:203], 0
	v_mfma_i32_16x16x64_i8 v[2:5], v[98:101], v[200:203], 0
	v_mfma_i32_16x16x64_i8 v[54:57], v[94:97], v[180:183], v[54:57]
	v_mfma_i32_16x16x64_i8 v[50:53], v[102:105], v[180:183], v[50:53]
	v_mfma_i32_16x16x64_i8 v[38:41], v[94:97], v[188:191], v[38:41]
	v_mfma_i32_16x16x64_i8 v[34:37], v[102:105], v[188:191], v[34:37]
	v_mfma_i32_16x16x64_i8 v[22:25], v[94:97], v[196:199], v[22:25]
	v_mfma_i32_16x16x64_i8 v[18:21], v[102:105], v[196:199], v[18:21]
	v_mfma_i32_16x16x64_i8 v[6:9], v[94:97], v[204:207], v[6:9]
	v_mfma_i32_16x16x64_i8 v[2:5], v[102:105], v[204:207], v[2:5]
	s_setprio 0
	s_barrier
	s_add_i32 s62, 0, 0x18000
	v_add_u32_e32 v0, s62, v227
	s_add_i32 s63, 0, 0x1c000
	ds_read_b128 v[66:69], v0
	ds_read_b128 v[70:73], v0 offset:1024
	ds_read_b128 v[82:85], v0 offset:2048
	ds_read_b128 v[86:89], v0 offset:3072
	v_add_u32_e32 v0, s63, v227
	ds_read_b128 v[90:93], v0
	ds_read_b128 v[94:97], v0 offset:1024
	ds_read_b128 v[98:101], v0 offset:2048
	ds_read_b128 v[102:105], v0 offset:3072
	s_add_u32 s42, s42, 0x40000
	s_addc_u32 s43, s43, 0
	s_mov_b32 m0, s49
	v_lshl_add_u64 v[216:217], s[42:43], 0, v[162:163]
	ds_read_b128 v[176:179], v231 offset:32768
	ds_read_b128 v[180:183], v231 offset:33792
	ds_read_b128 v[184:187], v231 offset:34816
	ds_read_b128 v[188:191], v231 offset:35840
	ds_read_b128 v[192:195], v231 offset:36864
	ds_read_b128 v[196:199], v231 offset:37888
	ds_read_b128 v[200:203], v231 offset:38912
	ds_read_b128 v[204:207], v231 offset:39936
	global_load_lds_dwordx4 v[216:217], off
	v_lshl_add_u64 v[216:217], s[42:43], 0, v[166:167]
	s_mov_b32 m0, s51
	s_nop 0
	global_load_lds_dwordx4 v[216:217], off
	s_waitcnt vmcnt(8)
	s_waitcnt lgkmcnt(0)
	s_barrier
	s_setprio 1
	s_waitcnt lgkmcnt(0)
	v_mfma_i32_16x16x64_i8 v[158:161], v[66:69], v[176:179], v[158:161]
	v_mfma_i32_16x16x64_i8 v[154:157], v[82:85], v[176:179], v[154:157]
	v_mfma_i32_16x16x64_i8 v[142:145], v[66:69], v[184:187], v[142:145]
	v_mfma_i32_16x16x64_i8 v[138:141], v[82:85], v[184:187], v[138:141]
	v_mfma_i32_16x16x64_i8 v[126:129], v[66:69], v[192:195], v[126:129]
	v_mfma_i32_16x16x64_i8 v[122:125], v[82:85], v[192:195], v[122:125]
	v_mfma_i32_16x16x64_i8 v[110:113], v[66:69], v[200:203], v[110:113]
	v_mfma_i32_16x16x64_i8 v[106:109], v[82:85], v[200:203], v[106:109]
	v_mfma_i32_16x16x64_i8 v[158:161], v[70:73], v[180:183], v[158:161]
	v_mfma_i32_16x16x64_i8 v[154:157], v[86:89], v[180:183], v[154:157]
	v_mfma_i32_16x16x64_i8 v[142:145], v[70:73], v[188:191], v[142:145]
	v_mfma_i32_16x16x64_i8 v[138:141], v[86:89], v[188:191], v[138:141]
	v_mfma_i32_16x16x64_i8 v[126:129], v[70:73], v[196:199], v[126:129]
	v_mfma_i32_16x16x64_i8 v[122:125], v[86:89], v[196:199], v[122:125]
	v_mfma_i32_16x16x64_i8 v[110:113], v[70:73], v[204:207], v[110:113]
	v_mfma_i32_16x16x64_i8 v[106:109], v[86:89], v[204:207], v[106:109]
	s_setprio 0
	s_setprio 1
	v_mfma_i32_16x16x64_i8 v[150:153], v[90:93], v[176:179], v[150:153]
	v_mfma_i32_16x16x64_i8 v[146:149], v[98:101], v[176:179], v[146:149]
	v_mfma_i32_16x16x64_i8 v[134:137], v[90:93], v[184:187], v[134:137]
	v_mfma_i32_16x16x64_i8 v[130:133], v[98:101], v[184:187], v[130:133]
	v_mfma_i32_16x16x64_i8 v[118:121], v[90:93], v[192:195], v[118:121]
	v_mfma_i32_16x16x64_i8 v[114:117], v[98:101], v[192:195], v[114:117]
	v_mfma_i32_16x16x64_i8 v[78:81], v[90:93], v[200:203], v[78:81]
	v_mfma_i32_16x16x64_i8 v[74:77], v[98:101], v[200:203], v[74:77]
	v_mfma_i32_16x16x64_i8 v[150:153], v[94:97], v[180:183], v[150:153]
	v_mfma_i32_16x16x64_i8 v[146:149], v[102:105], v[180:183], v[146:149]
	v_mfma_i32_16x16x64_i8 v[134:137], v[94:97], v[188:191], v[134:137]
	v_mfma_i32_16x16x64_i8 v[130:133], v[102:105], v[188:191], v[130:133]
	v_mfma_i32_16x16x64_i8 v[118:121], v[94:97], v[196:199], v[118:121]
	v_mfma_i32_16x16x64_i8 v[114:117], v[102:105], v[196:199], v[114:117]
	v_mfma_i32_16x16x64_i8 v[78:81], v[94:97], v[204:207], v[78:81]
	v_mfma_i32_16x16x64_i8 v[74:77], v[102:105], v[204:207], v[74:77]
	s_setprio 0
	s_barrier
	s_add_i32 s42, s62, s47
	v_lshl_add_u64 v[208:209], v[208:209], 0, s[22:23]
	s_mov_b32 m0, s42
	ds_read_b128 v[176:179], v231 offset:49152
	ds_read_b128 v[180:183], v231 offset:50176
	ds_read_b128 v[184:187], v231 offset:51200
	ds_read_b128 v[188:191], v231 offset:52224
	ds_read_b128 v[192:195], v231 offset:53248
	ds_read_b128 v[196:199], v231 offset:54272
	ds_read_b128 v[200:203], v231 offset:55296
	ds_read_b128 v[204:207], v231 offset:56320
	global_load_lds_dwordx4 v[208:209], off
	s_add_i32 m0, s42, 0x2000
	s_add_u32 s40, s40, 0x40080
	v_lshl_add_u64 v[208:209], v[210:211], 0, s[22:23]
	s_addc_u32 s41, s41, 0
	s_add_i32 s42, s63, s47
	global_load_lds_dwordx4 v[208:209], off
	v_lshl_add_u64 v[208:209], s[40:41], 0, v[164:165]
	s_mov_b32 m0, s42
	s_nop 0
	global_load_lds_dwordx4 v[208:209], off
	v_lshl_add_u64 v[208:209], s[40:41], 0, v[168:169]
	s_add_i32 m0, s42, 0x2000
	s_nop 0
	global_load_lds_dwordx4 v[208:209], off
	v_lshl_add_u64 v[208:209], v[212:213], 0, s[22:23]
	s_mov_b32 m0, s53
	s_nop 0
	global_load_lds_dwordx4 v[208:209], off
	v_lshl_add_u64 v[208:209], v[214:215], 0, s[22:23]
	s_mov_b32 m0, s54
	s_nop 0
	global_load_lds_dwordx4 v[208:209], off
	s_waitcnt vmcnt(8)
	s_waitcnt lgkmcnt(0)
	s_barrier
	s_setprio 1
	s_waitcnt lgkmcnt(0)
	v_mfma_i32_16x16x64_i8 v[62:65], v[66:69], v[176:179], v[62:65]
	v_mfma_i32_16x16x64_i8 v[58:61], v[82:85], v[176:179], v[58:61]
	v_mfma_i32_16x16x64_i8 v[46:49], v[66:69], v[184:187], v[46:49]
	v_mfma_i32_16x16x64_i8 v[42:45], v[82:85], v[184:187], v[42:45]
	v_mfma_i32_16x16x64_i8 v[30:33], v[66:69], v[192:195], v[30:33]
	v_mfma_i32_16x16x64_i8 v[26:29], v[82:85], v[192:195], v[26:29]
	v_mfma_i32_16x16x64_i8 v[14:17], v[66:69], v[200:203], v[14:17]
	v_mfma_i32_16x16x64_i8 v[10:13], v[82:85], v[200:203], v[10:13]
	v_mfma_i32_16x16x64_i8 v[62:65], v[70:73], v[180:183], v[62:65]
	v_mfma_i32_16x16x64_i8 v[58:61], v[86:89], v[180:183], v[58:61]
	v_mfma_i32_16x16x64_i8 v[46:49], v[70:73], v[188:191], v[46:49]
	v_mfma_i32_16x16x64_i8 v[42:45], v[86:89], v[188:191], v[42:45]
	v_mfma_i32_16x16x64_i8 v[30:33], v[70:73], v[196:199], v[30:33]
	v_mfma_i32_16x16x64_i8 v[26:29], v[86:89], v[196:199], v[26:29]
	v_mfma_i32_16x16x64_i8 v[14:17], v[70:73], v[204:207], v[14:17]
	v_mfma_i32_16x16x64_i8 v[10:13], v[86:89], v[204:207], v[10:13]
	s_setprio 0
	s_setprio 1
	v_mfma_i32_16x16x64_i8 v[54:57], v[90:93], v[176:179], v[54:57]
	v_mfma_i32_16x16x64_i8 v[50:53], v[98:101], v[176:179], v[50:53]
	v_mfma_i32_16x16x64_i8 v[38:41], v[90:93], v[184:187], v[38:41]
	v_mfma_i32_16x16x64_i8 v[34:37], v[98:101], v[184:187], v[34:37]
	v_mfma_i32_16x16x64_i8 v[22:25], v[90:93], v[192:195], v[22:25]
	v_mfma_i32_16x16x64_i8 v[18:21], v[98:101], v[192:195], v[18:21]
	v_mfma_i32_16x16x64_i8 v[6:9], v[90:93], v[200:203], v[6:9]
	v_mfma_i32_16x16x64_i8 v[2:5], v[98:101], v[200:203], v[2:5]
	v_mfma_i32_16x16x64_i8 v[54:57], v[94:97], v[180:183], v[54:57]
	v_mfma_i32_16x16x64_i8 v[50:53], v[102:105], v[180:183], v[50:53]
	v_mfma_i32_16x16x64_i8 v[38:41], v[94:97], v[188:191], v[38:41]
	v_mfma_i32_16x16x64_i8 v[34:37], v[102:105], v[188:191], v[34:37]
	v_mfma_i32_16x16x64_i8 v[22:25], v[94:97], v[196:199], v[22:25]
	v_mfma_i32_16x16x64_i8 v[18:21], v[102:105], v[196:199], v[18:21]
	v_mfma_i32_16x16x64_i8 v[6:9], v[94:97], v[204:207], v[6:9]
	v_mfma_i32_16x16x64_i8 v[2:5], v[102:105], v[204:207], v[2:5]
	s_setprio 0
	s_barrier
	s_add_i32 s61, s61, 2
	s_add_u32 s0, s0, 0x100
	s_addc_u32 s1, s1, 0
	s_add_u32 s31, s31, 0x100
	s_addc_u32 s39, s39, 0
	s_cmp_gt_u32 s61, 13
	s_cbranch_scc0 .LBB0_1367
	s_branch .Lkexit_1367
	s_nop 0
	s_nop 0
	s_nop 0
	s_nop 0
	s_nop 0
	s_nop 0
	s_nop 0
	s_nop 0

.Lkexit_1367:
	s_and_b64 vcc, exec, s[24:25]
	s_cbranch_vccz .LBB0_1370
	s_barrier
